# P0 adaLN GEMV: K loop fully unrolled, all 32 weight loads of a unit issued up front into unused registers with counted vmcnt per iteration
# speedup vs baseline: 1.0307x; 1.0079x over previous
; __device__ __forceinline__ void p0_ada(Frame& F, const float* c, const float* ada_w, const float* ada_b, float* mod) {
;     ...
;     for (int u = blockIdx.x; u < 768; u += F.G) {
;         const int l = u / 384, cb = u % 384;
;         const float* W = ada_w + (size_t)l * D * 6 * D + cb * 32 + cq * 4;
;         f32x4 acc[8];
; #pragma unroll
;         for (int b = 0; b < 8; ++b) acc[b] = (f32x4){0.f, 0.f, 0.f, 0.f};
;         const int kbase = F.wave * 256 + ks;
; #pragma unroll 4
;         for (int it = 0; it < 32; ++it) {
;             const int k = kbase + 8 * it;
;             const f32x4 w = __builtin_nontemporal_load((const f32x4*)(W + (size_t)k * 6 * D));
;             const f32x4 c0 = *(const f32x4*)(cond + k * 8), c1 = *(const f32x4*)(cond + k * 8 + 4);
;             acc[0] += w * c0[0]; acc[1] += w * c0[1]; acc[2] += w * c0[2]; acc[3] += w * c0[3];
;             acc[4] += w * c1[0]; acc[5] += w * c1[1]; acc[6] += w * c1[2]; acc[7] += w * c1[3];
;         }
.LBB0_20:
	v_mov_b32_e32 v244, v77
	v_add_u32_e32 v245, 8, v244
	v_add_u32_e32 v246, 16, v244
	v_add_u32_e32 v247, 24, v244
	v_mad_u64_u32 v[248:249], s[18:19], v244, s15, v[42:43]
	v_mad_u64_u32 v[250:251], s[18:19], v245, s15, v[42:43]
	v_mad_u64_u32 v[252:253], s[18:19], v246, s15, v[42:43]
	v_mad_u64_u32 v[244:245], s[18:19], v247, s15, v[42:43]
	global_load_dwordx4 v[114:117], v[248:249], off nt
	global_load_dwordx4 v[118:121], v[250:251], off nt
	global_load_dwordx4 v[122:125], v[252:253], off nt
	global_load_dwordx4 v[126:129], v[244:245], off nt
	v_add_u32_e32 v244, 0x20, v77
	v_add_u32_e32 v245, 8, v244
	v_add_u32_e32 v246, 16, v244
	v_add_u32_e32 v247, 24, v244
	v_mad_u64_u32 v[248:249], s[18:19], v244, s15, v[42:43]
	v_mad_u64_u32 v[250:251], s[18:19], v245, s15, v[42:43]
	v_mad_u64_u32 v[252:253], s[18:19], v246, s15, v[42:43]
	v_mad_u64_u32 v[244:245], s[18:19], v247, s15, v[42:43]
	global_load_dwordx4 v[130:133], v[248:249], off nt
	global_load_dwordx4 v[134:137], v[250:251], off nt
	global_load_dwordx4 v[138:141], v[252:253], off nt
	global_load_dwordx4 v[142:145], v[244:245], off nt
	v_add_u32_e32 v244, 0x40, v77
	v_add_u32_e32 v245, 8, v244
	v_add_u32_e32 v246, 16, v244
	v_add_u32_e32 v247, 24, v244
	v_mad_u64_u32 v[248:249], s[18:19], v244, s15, v[42:43]
	v_mad_u64_u32 v[250:251], s[18:19], v245, s15, v[42:43]
	v_mad_u64_u32 v[252:253], s[18:19], v246, s15, v[42:43]
	v_mad_u64_u32 v[244:245], s[18:19], v247, s15, v[42:43]
	global_load_dwordx4 v[146:149], v[248:249], off nt
	global_load_dwordx4 v[150:153], v[250:251], off nt
	global_load_dwordx4 v[154:157], v[252:253], off nt
	global_load_dwordx4 v[158:161], v[244:245], off nt
	v_add_u32_e32 v244, 0x60, v77
	v_add_u32_e32 v245, 8, v244
	v_add_u32_e32 v246, 16, v244
	v_add_u32_e32 v247, 24, v244
	v_mad_u64_u32 v[248:249], s[18:19], v244, s15, v[42:43]
	v_mad_u64_u32 v[250:251], s[18:19], v245, s15, v[42:43]
	v_mad_u64_u32 v[252:253], s[18:19], v246, s15, v[42:43]
	v_mad_u64_u32 v[244:245], s[18:19], v247, s15, v[42:43]
	global_load_dwordx4 v[162:165], v[248:249], off nt
	global_load_dwordx4 v[166:169], v[250:251], off nt
	global_load_dwordx4 v[170:173], v[252:253], off nt
	global_load_dwordx4 v[174:177], v[244:245], off nt
	v_add_u32_e32 v244, 0x80, v77
	v_add_u32_e32 v245, 8, v244
	v_add_u32_e32 v246, 16, v244
	v_add_u32_e32 v247, 24, v244
	v_mad_u64_u32 v[248:249], s[18:19], v244, s15, v[42:43]
	v_mad_u64_u32 v[250:251], s[18:19], v245, s15, v[42:43]
	v_mad_u64_u32 v[252:253], s[18:19], v246, s15, v[42:43]
	v_mad_u64_u32 v[244:245], s[18:19], v247, s15, v[42:43]
	global_load_dwordx4 v[178:181], v[248:249], off nt
	global_load_dwordx4 v[182:185], v[250:251], off nt
	global_load_dwordx4 v[186:189], v[252:253], off nt
	global_load_dwordx4 v[190:193], v[244:245], off nt
	v_add_u32_e32 v244, 0xa0, v77
	v_add_u32_e32 v245, 8, v244
	v_add_u32_e32 v246, 16, v244
	v_add_u32_e32 v247, 24, v244
	v_mad_u64_u32 v[248:249], s[18:19], v244, s15, v[42:43]
	v_mad_u64_u32 v[250:251], s[18:19], v245, s15, v[42:43]
	v_mad_u64_u32 v[252:253], s[18:19], v246, s15, v[42:43]
	v_mad_u64_u32 v[244:245], s[18:19], v247, s15, v[42:43]
	global_load_dwordx4 v[196:199], v[248:249], off nt
	global_load_dwordx4 v[200:203], v[250:251], off nt
	global_load_dwordx4 v[204:207], v[252:253], off nt
	global_load_dwordx4 v[208:211], v[244:245], off nt
	v_add_u32_e32 v244, 0xc0, v77
	v_add_u32_e32 v245, 8, v244
	v_add_u32_e32 v246, 16, v244
	v_add_u32_e32 v247, 24, v244
	v_mad_u64_u32 v[248:249], s[18:19], v244, s15, v[42:43]
	v_mad_u64_u32 v[250:251], s[18:19], v245, s15, v[42:43]
	v_mad_u64_u32 v[252:253], s[18:19], v246, s15, v[42:43]
	v_mad_u64_u32 v[244:245], s[18:19], v247, s15, v[42:43]
	global_load_dwordx4 v[212:215], v[248:249], off nt
	global_load_dwordx4 v[216:219], v[250:251], off nt
	global_load_dwordx4 v[220:223], v[252:253], off nt
	global_load_dwordx4 v[224:227], v[244:245], off nt
	v_add_u32_e32 v244, 0xe0, v77
	v_add_u32_e32 v245, 8, v244
	v_add_u32_e32 v246, 16, v244
	v_add_u32_e32 v247, 24, v244
	v_mad_u64_u32 v[248:249], s[18:19], v244, s15, v[42:43]
	v_mad_u64_u32 v[250:251], s[18:19], v245, s15, v[42:43]
	v_mad_u64_u32 v[252:253], s[18:19], v246, s15, v[42:43]
	v_mad_u64_u32 v[244:245], s[18:19], v247, s15, v[42:43]
	global_load_dwordx4 v[228:231], v[248:249], off nt
	global_load_dwordx4 v[232:235], v[250:251], off nt
	global_load_dwordx4 v[236:239], v[252:253], off nt
	global_load_dwordx4 v[240:243], v[244:245], off nt
	ds_read_b128 v[6:9], v50
	ds_read_b128 v[2:5], v50 offset:16
	ds_read_b128 v[52:55], v50 offset:256
	ds_read_b128 v[78:81], v50 offset:272
	ds_read_b128 v[82:85], v50 offset:512
	ds_read_b128 v[86:89], v50 offset:528
	ds_read_b128 v[90:93], v50 offset:768
	ds_read_b128 v[94:97], v50 offset:784
	s_waitcnt lgkmcnt(0)
	v_mov_b32_e32 v98, v9
	v_mov_b32_e32 v100, v5
	v_mov_b32_e32 v102, v55
	v_mov_b32_e32 v104, v81
	v_mov_b32_e32 v106, v85
	v_mov_b32_e32 v108, v89
	s_add_i32 s12, s12, 32
	v_mov_b32_e32 v110, v93
	v_mov_b32_e32 v112, v97
	v_add_u32_e32 v50, 0x400, v50
	s_cmpk_lg_i32 s12, 0x100
	s_waitcnt vmcnt(28)
; __device__ __forceinline__ void p0_ada(Frame& F, const float* c, const float* ada_w, const float* ada_b, float* mod) {
;     ...
;         for (int it = 0; it < 32; ++it) {
;             const int k = kbase + 8 * it;
;             const f32x4 w = __builtin_nontemporal_load((const f32x4*)(W + (size_t)k * 6 * D));
;             const f32x4 c0 = *(const f32x4*)(cond + k * 8), c1 = *(const f32x4*)(cond + k * 8 + 4);
;             acc[0] += w * c0[0]; acc[1] += w * c0[1]; acc[2] += w * c0[2]; acc[3] += w * c0[3];
;             acc[4] += w * c1[0]; acc[5] += w * c1[1]; acc[6] += w * c1[2]; acc[7] += w * c1[3];
;         }
	v_pk_fma_f32 v[48:49], v[114:115], v[6:7], v[48:49] op_sel_hi:[1,0,1]
	v_pk_fma_f32 v[46:47], v[116:117], v[6:7], v[46:47] op_sel_hi:[1,0,1]
	v_pk_fma_f32 v[44:45], v[114:115], v[6:7], v[44:45] op_sel:[0,1,0]
	v_pk_fma_f32 v[6:7], v[116:117], v[6:7], v[40:41] op_sel:[0,1,0]
	v_pk_fma_f32 v[38:39], v[114:115], v[8:9], v[38:39] op_sel_hi:[1,0,1]
	v_pk_fma_f32 v[8:9], v[116:117], v[8:9], v[36:37] op_sel_hi:[1,0,1]
	v_pk_fma_f32 v[30:31], v[114:115], v[2:3], v[30:31] op_sel_hi:[1,0,1]
	v_pk_fma_f32 v[28:29], v[116:117], v[2:3], v[28:29] op_sel_hi:[1,0,1]
	v_pk_fma_f32 v[26:27], v[114:115], v[2:3], v[26:27] op_sel:[0,1,0]
	v_pk_fma_f32 v[2:3], v[116:117], v[2:3], v[24:25] op_sel:[0,1,0]
	v_pk_fma_f32 v[22:23], v[114:115], v[4:5], v[22:23] op_sel_hi:[1,0,1]
	v_pk_fma_f32 v[4:5], v[116:117], v[4:5], v[20:21] op_sel_hi:[1,0,1]
	v_pk_fma_f32 v[20:21], v[114:115], v[98:99], v[34:35] op_sel_hi:[1,0,1]
	v_pk_fma_f32 v[24:25], v[116:117], v[98:99], v[32:33] op_sel_hi:[1,0,1]
	v_pk_fma_f32 v[18:19], v[114:115], v[100:101], v[18:19] op_sel_hi:[1,0,1]
	v_pk_fma_f32 v[16:17], v[116:117], v[100:101], v[16:17] op_sel_hi:[1,0,1]
	v_pk_fma_f32 v[32:33], v[120:121], v[52:53], v[46:47] op_sel_hi:[1,0,1]
	v_pk_fma_f32 v[34:35], v[118:119], v[52:53], v[48:49] op_sel_hi:[1,0,1]
	v_pk_fma_f32 v[6:7], v[120:121], v[52:53], v[6:7] op_sel:[0,1,0]
	v_pk_fma_f32 v[36:37], v[118:119], v[52:53], v[44:45] op_sel:[0,1,0]
	v_pk_fma_f32 v[8:9], v[120:121], v[54:55], v[8:9] op_sel_hi:[1,0,1]
	v_pk_fma_f32 v[38:39], v[118:119], v[54:55], v[38:39] op_sel_hi:[1,0,1]
	v_pk_fma_f32 v[28:29], v[120:121], v[78:79], v[28:29] op_sel_hi:[1,0,1]
	v_pk_fma_f32 v[30:31], v[118:119], v[78:79], v[30:31] op_sel_hi:[1,0,1]
	v_pk_fma_f32 v[2:3], v[120:121], v[78:79], v[2:3] op_sel:[0,1,0]
	v_pk_fma_f32 v[26:27], v[118:119], v[78:79], v[26:27] op_sel:[0,1,0]
	v_pk_fma_f32 v[4:5], v[120:121], v[80:81], v[4:5] op_sel_hi:[1,0,1]
	v_pk_fma_f32 v[22:23], v[118:119], v[80:81], v[22:23] op_sel_hi:[1,0,1]
	v_pk_fma_f32 v[24:25], v[120:121], v[102:103], v[24:25] op_sel_hi:[1,0,1]
	v_pk_fma_f32 v[20:21], v[118:119], v[102:103], v[20:21] op_sel_hi:[1,0,1]
	v_pk_fma_f32 v[16:17], v[120:121], v[104:105], v[16:17] op_sel_hi:[1,0,1]
	v_pk_fma_f32 v[18:19], v[118:119], v[104:105], v[18:19] op_sel_hi:[1,0,1]
	v_pk_fma_f32 v[32:33], v[124:125], v[82:83], v[32:33] op_sel_hi:[1,0,1]
	v_pk_fma_f32 v[34:35], v[122:123], v[82:83], v[34:35] op_sel_hi:[1,0,1]
	v_pk_fma_f32 v[6:7], v[124:125], v[82:83], v[6:7] op_sel:[0,1,0]
	v_pk_fma_f32 v[36:37], v[122:123], v[82:83], v[36:37] op_sel:[0,1,0]
	v_pk_fma_f32 v[38:39], v[122:123], v[84:85], v[38:39] op_sel_hi:[1,0,1]
	v_pk_fma_f32 v[8:9], v[124:125], v[84:85], v[8:9] op_sel_hi:[1,0,1]
	v_pk_fma_f32 v[28:29], v[124:125], v[86:87], v[28:29] op_sel_hi:[1,0,1]
	v_pk_fma_f32 v[30:31], v[122:123], v[86:87], v[30:31] op_sel_hi:[1,0,1]
	v_pk_fma_f32 v[2:3], v[124:125], v[86:87], v[2:3] op_sel:[0,1,0]
	v_pk_fma_f32 v[26:27], v[122:123], v[86:87], v[26:27] op_sel:[0,1,0]
	v_pk_fma_f32 v[22:23], v[122:123], v[88:89], v[22:23] op_sel_hi:[1,0,1]
	v_pk_fma_f32 v[4:5], v[124:125], v[88:89], v[4:5] op_sel_hi:[1,0,1]
	v_pk_fma_f32 v[20:21], v[122:123], v[106:107], v[20:21] op_sel_hi:[1,0,1]
	v_pk_fma_f32 v[24:25], v[124:125], v[106:107], v[24:25] op_sel_hi:[1,0,1]
	v_pk_fma_f32 v[18:19], v[122:123], v[108:109], v[18:19] op_sel_hi:[1,0,1]
	v_pk_fma_f32 v[16:17], v[124:125], v[108:109], v[16:17] op_sel_hi:[1,0,1]
	v_pk_fma_f32 v[46:47], v[128:129], v[90:91], v[32:33] op_sel_hi:[1,0,1]
	v_pk_fma_f32 v[48:49], v[126:127], v[90:91], v[34:35] op_sel_hi:[1,0,1]
	v_pk_fma_f32 v[40:41], v[128:129], v[90:91], v[6:7] op_sel:[0,1,0]
	v_pk_fma_f32 v[44:45], v[126:127], v[90:91], v[36:37] op_sel:[0,1,0]
	v_pk_fma_f32 v[36:37], v[128:129], v[92:93], v[8:9] op_sel_hi:[1,0,1]
	v_pk_fma_f32 v[38:39], v[126:127], v[92:93], v[38:39] op_sel_hi:[1,0,1]
	v_pk_fma_f32 v[32:33], v[128:129], v[110:111], v[24:25] op_sel_hi:[1,0,1]
	v_pk_fma_f32 v[34:35], v[126:127], v[110:111], v[20:21] op_sel_hi:[1,0,1]
	v_pk_fma_f32 v[28:29], v[128:129], v[94:95], v[28:29] op_sel_hi:[1,0,1]
	v_pk_fma_f32 v[30:31], v[126:127], v[94:95], v[30:31] op_sel_hi:[1,0,1]
	v_pk_fma_f32 v[24:25], v[128:129], v[94:95], v[2:3] op_sel:[0,1,0]
	v_pk_fma_f32 v[26:27], v[126:127], v[94:95], v[26:27] op_sel:[0,1,0]
	v_pk_fma_f32 v[20:21], v[128:129], v[96:97], v[4:5] op_sel_hi:[1,0,1]
	v_pk_fma_f32 v[22:23], v[126:127], v[96:97], v[22:23] op_sel_hi:[1,0,1]
	v_pk_fma_f32 v[16:17], v[128:129], v[112:113], v[16:17] op_sel_hi:[1,0,1]
	v_pk_fma_f32 v[18:19], v[126:127], v[112:113], v[18:19] op_sel_hi:[1,0,1]
	ds_read_b128 v[6:9], v50
	ds_read_b128 v[2:5], v50 offset:16
	ds_read_b128 v[52:55], v50 offset:256
	ds_read_b128 v[78:81], v50 offset:272
	ds_read_b128 v[82:85], v50 offset:512
	ds_read_b128 v[86:89], v50 offset:528
	ds_read_b128 v[90:93], v50 offset:768
	ds_read_b128 v[94:97], v50 offset:784
	s_waitcnt lgkmcnt(0)
	v_mov_b32_e32 v98, v9
	v_mov_b32_e32 v100, v5
	v_mov_b32_e32 v102, v55
	v_mov_b32_e32 v104, v81
	v_mov_b32_e32 v106, v85
	v_mov_b32_e32 v108, v89
	s_add_i32 s12, s12, 32
	v_mov_b32_e32 v110, v93
	v_mov_b32_e32 v112, v97
	v_add_u32_e32 v50, 0x400, v50
	s_cmpk_lg_i32 s12, 0x100
	s_waitcnt vmcnt(24)
; __device__ __forceinline__ void p0_ada(Frame& F, const float* c, const float* ada_w, const float* ada_b, float* mod) {
;     ...
;         for (int it = 0; it < 32; ++it) {
;             const int k = kbase + 8 * it;
;             const f32x4 w = __builtin_nontemporal_load((const f32x4*)(W + (size_t)k * 6 * D));
;             const f32x4 c0 = *(const f32x4*)(cond + k * 8), c1 = *(const f32x4*)(cond + k * 8 + 4);
;             acc[0] += w * c0[0]; acc[1] += w * c0[1]; acc[2] += w * c0[2]; acc[3] += w * c0[3];
;             acc[4] += w * c1[0]; acc[5] += w * c1[1]; acc[6] += w * c1[2]; acc[7] += w * c1[3];
;         }
	v_pk_fma_f32 v[48:49], v[130:131], v[6:7], v[48:49] op_sel_hi:[1,0,1]
	v_pk_fma_f32 v[46:47], v[132:133], v[6:7], v[46:47] op_sel_hi:[1,0,1]
	v_pk_fma_f32 v[44:45], v[130:131], v[6:7], v[44:45] op_sel:[0,1,0]
	v_pk_fma_f32 v[6:7], v[132:133], v[6:7], v[40:41] op_sel:[0,1,0]
	v_pk_fma_f32 v[38:39], v[130:131], v[8:9], v[38:39] op_sel_hi:[1,0,1]
	v_pk_fma_f32 v[8:9], v[132:133], v[8:9], v[36:37] op_sel_hi:[1,0,1]
	v_pk_fma_f32 v[30:31], v[130:131], v[2:3], v[30:31] op_sel_hi:[1,0,1]
	v_pk_fma_f32 v[28:29], v[132:133], v[2:3], v[28:29] op_sel_hi:[1,0,1]
	v_pk_fma_f32 v[26:27], v[130:131], v[2:3], v[26:27] op_sel:[0,1,0]
	v_pk_fma_f32 v[2:3], v[132:133], v[2:3], v[24:25] op_sel:[0,1,0]
	v_pk_fma_f32 v[22:23], v[130:131], v[4:5], v[22:23] op_sel_hi:[1,0,1]
	v_pk_fma_f32 v[4:5], v[132:133], v[4:5], v[20:21] op_sel_hi:[1,0,1]
	v_pk_fma_f32 v[20:21], v[130:131], v[98:99], v[34:35] op_sel_hi:[1,0,1]
	v_pk_fma_f32 v[24:25], v[132:133], v[98:99], v[32:33] op_sel_hi:[1,0,1]
	v_pk_fma_f32 v[18:19], v[130:131], v[100:101], v[18:19] op_sel_hi:[1,0,1]
	v_pk_fma_f32 v[16:17], v[132:133], v[100:101], v[16:17] op_sel_hi:[1,0,1]
	v_pk_fma_f32 v[32:33], v[136:137], v[52:53], v[46:47] op_sel_hi:[1,0,1]
	v_pk_fma_f32 v[34:35], v[134:135], v[52:53], v[48:49] op_sel_hi:[1,0,1]
	v_pk_fma_f32 v[6:7], v[136:137], v[52:53], v[6:7] op_sel:[0,1,0]
	v_pk_fma_f32 v[36:37], v[134:135], v[52:53], v[44:45] op_sel:[0,1,0]
	v_pk_fma_f32 v[8:9], v[136:137], v[54:55], v[8:9] op_sel_hi:[1,0,1]
	v_pk_fma_f32 v[38:39], v[134:135], v[54:55], v[38:39] op_sel_hi:[1,0,1]
	v_pk_fma_f32 v[28:29], v[136:137], v[78:79], v[28:29] op_sel_hi:[1,0,1]
	v_pk_fma_f32 v[30:31], v[134:135], v[78:79], v[30:31] op_sel_hi:[1,0,1]
	v_pk_fma_f32 v[2:3], v[136:137], v[78:79], v[2:3] op_sel:[0,1,0]
	v_pk_fma_f32 v[26:27], v[134:135], v[78:79], v[26:27] op_sel:[0,1,0]
	v_pk_fma_f32 v[4:5], v[136:137], v[80:81], v[4:5] op_sel_hi:[1,0,1]
	v_pk_fma_f32 v[22:23], v[134:135], v[80:81], v[22:23] op_sel_hi:[1,0,1]
	v_pk_fma_f32 v[24:25], v[136:137], v[102:103], v[24:25] op_sel_hi:[1,0,1]
	v_pk_fma_f32 v[20:21], v[134:135], v[102:103], v[20:21] op_sel_hi:[1,0,1]
	v_pk_fma_f32 v[16:17], v[136:137], v[104:105], v[16:17] op_sel_hi:[1,0,1]
	v_pk_fma_f32 v[18:19], v[134:135], v[104:105], v[18:19] op_sel_hi:[1,0,1]
	v_pk_fma_f32 v[32:33], v[140:141], v[82:83], v[32:33] op_sel_hi:[1,0,1]
	v_pk_fma_f32 v[34:35], v[138:139], v[82:83], v[34:35] op_sel_hi:[1,0,1]
	v_pk_fma_f32 v[6:7], v[140:141], v[82:83], v[6:7] op_sel:[0,1,0]
	v_pk_fma_f32 v[36:37], v[138:139], v[82:83], v[36:37] op_sel:[0,1,0]
	v_pk_fma_f32 v[38:39], v[138:139], v[84:85], v[38:39] op_sel_hi:[1,0,1]
	v_pk_fma_f32 v[8:9], v[140:141], v[84:85], v[8:9] op_sel_hi:[1,0,1]
	v_pk_fma_f32 v[28:29], v[140:141], v[86:87], v[28:29] op_sel_hi:[1,0,1]
	v_pk_fma_f32 v[30:31], v[138:139], v[86:87], v[30:31] op_sel_hi:[1,0,1]
	v_pk_fma_f32 v[2:3], v[140:141], v[86:87], v[2:3] op_sel:[0,1,0]
	v_pk_fma_f32 v[26:27], v[138:139], v[86:87], v[26:27] op_sel:[0,1,0]
	v_pk_fma_f32 v[22:23], v[138:139], v[88:89], v[22:23] op_sel_hi:[1,0,1]
	v_pk_fma_f32 v[4:5], v[140:141], v[88:89], v[4:5] op_sel_hi:[1,0,1]
	v_pk_fma_f32 v[20:21], v[138:139], v[106:107], v[20:21] op_sel_hi:[1,0,1]
	v_pk_fma_f32 v[24:25], v[140:141], v[106:107], v[24:25] op_sel_hi:[1,0,1]
	v_pk_fma_f32 v[18:19], v[138:139], v[108:109], v[18:19] op_sel_hi:[1,0,1]
	v_pk_fma_f32 v[16:17], v[140:141], v[108:109], v[16:17] op_sel_hi:[1,0,1]
	v_pk_fma_f32 v[46:47], v[144:145], v[90:91], v[32:33] op_sel_hi:[1,0,1]
	v_pk_fma_f32 v[48:49], v[142:143], v[90:91], v[34:35] op_sel_hi:[1,0,1]
	v_pk_fma_f32 v[40:41], v[144:145], v[90:91], v[6:7] op_sel:[0,1,0]
	v_pk_fma_f32 v[44:45], v[142:143], v[90:91], v[36:37] op_sel:[0,1,0]
	v_pk_fma_f32 v[36:37], v[144:145], v[92:93], v[8:9] op_sel_hi:[1,0,1]
	v_pk_fma_f32 v[38:39], v[142:143], v[92:93], v[38:39] op_sel_hi:[1,0,1]
	v_pk_fma_f32 v[32:33], v[144:145], v[110:111], v[24:25] op_sel_hi:[1,0,1]
	v_pk_fma_f32 v[34:35], v[142:143], v[110:111], v[20:21] op_sel_hi:[1,0,1]
	v_pk_fma_f32 v[28:29], v[144:145], v[94:95], v[28:29] op_sel_hi:[1,0,1]
	v_pk_fma_f32 v[30:31], v[142:143], v[94:95], v[30:31] op_sel_hi:[1,0,1]
	v_pk_fma_f32 v[24:25], v[144:145], v[94:95], v[2:3] op_sel:[0,1,0]
	v_pk_fma_f32 v[26:27], v[142:143], v[94:95], v[26:27] op_sel:[0,1,0]
	v_pk_fma_f32 v[20:21], v[144:145], v[96:97], v[4:5] op_sel_hi:[1,0,1]
	v_pk_fma_f32 v[22:23], v[142:143], v[96:97], v[22:23] op_sel_hi:[1,0,1]
	v_pk_fma_f32 v[16:17], v[144:145], v[112:113], v[16:17] op_sel_hi:[1,0,1]
	v_pk_fma_f32 v[18:19], v[142:143], v[112:113], v[18:19] op_sel_hi:[1,0,1]
	ds_read_b128 v[6:9], v50
	ds_read_b128 v[2:5], v50 offset:16
	ds_read_b128 v[52:55], v50 offset:256
	ds_read_b128 v[78:81], v50 offset:272
	ds_read_b128 v[82:85], v50 offset:512
	ds_read_b128 v[86:89], v50 offset:528
	ds_read_b128 v[90:93], v50 offset:768
	ds_read_b128 v[94:97], v50 offset:784
	s_waitcnt lgkmcnt(0)
	v_mov_b32_e32 v98, v9
	v_mov_b32_e32 v100, v5
	v_mov_b32_e32 v102, v55
	v_mov_b32_e32 v104, v81
	v_mov_b32_e32 v106, v85
	v_mov_b32_e32 v108, v89
	s_add_i32 s12, s12, 32
	v_mov_b32_e32 v110, v93
	v_mov_b32_e32 v112, v97
	v_add_u32_e32 v50, 0x400, v50
	s_cmpk_lg_i32 s12, 0x100
	s_waitcnt vmcnt(20)
; __device__ __forceinline__ void p0_ada(Frame& F, const float* c, const float* ada_w, const float* ada_b, float* mod) {
;     ...
;         for (int it = 0; it < 32; ++it) {
;             const int k = kbase + 8 * it;
;             const f32x4 w = __builtin_nontemporal_load((const f32x4*)(W + (size_t)k * 6 * D));
;             const f32x4 c0 = *(const f32x4*)(cond + k * 8), c1 = *(const f32x4*)(cond + k * 8 + 4);
;             acc[0] += w * c0[0]; acc[1] += w * c0[1]; acc[2] += w * c0[2]; acc[3] += w * c0[3];
;             acc[4] += w * c1[0]; acc[5] += w * c1[1]; acc[6] += w * c1[2]; acc[7] += w * c1[3];
;         }
	v_pk_fma_f32 v[48:49], v[146:147], v[6:7], v[48:49] op_sel_hi:[1,0,1]
	v_pk_fma_f32 v[46:47], v[148:149], v[6:7], v[46:47] op_sel_hi:[1,0,1]
	v_pk_fma_f32 v[44:45], v[146:147], v[6:7], v[44:45] op_sel:[0,1,0]
	v_pk_fma_f32 v[6:7], v[148:149], v[6:7], v[40:41] op_sel:[0,1,0]
	v_pk_fma_f32 v[38:39], v[146:147], v[8:9], v[38:39] op_sel_hi:[1,0,1]
	v_pk_fma_f32 v[8:9], v[148:149], v[8:9], v[36:37] op_sel_hi:[1,0,1]
	v_pk_fma_f32 v[30:31], v[146:147], v[2:3], v[30:31] op_sel_hi:[1,0,1]
	v_pk_fma_f32 v[28:29], v[148:149], v[2:3], v[28:29] op_sel_hi:[1,0,1]
	v_pk_fma_f32 v[26:27], v[146:147], v[2:3], v[26:27] op_sel:[0,1,0]
	v_pk_fma_f32 v[2:3], v[148:149], v[2:3], v[24:25] op_sel:[0,1,0]
	v_pk_fma_f32 v[22:23], v[146:147], v[4:5], v[22:23] op_sel_hi:[1,0,1]
	v_pk_fma_f32 v[4:5], v[148:149], v[4:5], v[20:21] op_sel_hi:[1,0,1]
	v_pk_fma_f32 v[20:21], v[146:147], v[98:99], v[34:35] op_sel_hi:[1,0,1]
	v_pk_fma_f32 v[24:25], v[148:149], v[98:99], v[32:33] op_sel_hi:[1,0,1]
	v_pk_fma_f32 v[18:19], v[146:147], v[100:101], v[18:19] op_sel_hi:[1,0,1]
	v_pk_fma_f32 v[16:17], v[148:149], v[100:101], v[16:17] op_sel_hi:[1,0,1]
	v_pk_fma_f32 v[32:33], v[152:153], v[52:53], v[46:47] op_sel_hi:[1,0,1]
	v_pk_fma_f32 v[34:35], v[150:151], v[52:53], v[48:49] op_sel_hi:[1,0,1]
	v_pk_fma_f32 v[6:7], v[152:153], v[52:53], v[6:7] op_sel:[0,1,0]
	v_pk_fma_f32 v[36:37], v[150:151], v[52:53], v[44:45] op_sel:[0,1,0]
	v_pk_fma_f32 v[8:9], v[152:153], v[54:55], v[8:9] op_sel_hi:[1,0,1]
	v_pk_fma_f32 v[38:39], v[150:151], v[54:55], v[38:39] op_sel_hi:[1,0,1]
	v_pk_fma_f32 v[28:29], v[152:153], v[78:79], v[28:29] op_sel_hi:[1,0,1]
	v_pk_fma_f32 v[30:31], v[150:151], v[78:79], v[30:31] op_sel_hi:[1,0,1]
	v_pk_fma_f32 v[2:3], v[152:153], v[78:79], v[2:3] op_sel:[0,1,0]
	v_pk_fma_f32 v[26:27], v[150:151], v[78:79], v[26:27] op_sel:[0,1,0]
	v_pk_fma_f32 v[4:5], v[152:153], v[80:81], v[4:5] op_sel_hi:[1,0,1]
	v_pk_fma_f32 v[22:23], v[150:151], v[80:81], v[22:23] op_sel_hi:[1,0,1]
	v_pk_fma_f32 v[24:25], v[152:153], v[102:103], v[24:25] op_sel_hi:[1,0,1]
	v_pk_fma_f32 v[20:21], v[150:151], v[102:103], v[20:21] op_sel_hi:[1,0,1]
	v_pk_fma_f32 v[16:17], v[152:153], v[104:105], v[16:17] op_sel_hi:[1,0,1]
	v_pk_fma_f32 v[18:19], v[150:151], v[104:105], v[18:19] op_sel_hi:[1,0,1]
	v_pk_fma_f32 v[32:33], v[156:157], v[82:83], v[32:33] op_sel_hi:[1,0,1]
	v_pk_fma_f32 v[34:35], v[154:155], v[82:83], v[34:35] op_sel_hi:[1,0,1]
	v_pk_fma_f32 v[6:7], v[156:157], v[82:83], v[6:7] op_sel:[0,1,0]
	v_pk_fma_f32 v[36:37], v[154:155], v[82:83], v[36:37] op_sel:[0,1,0]
	v_pk_fma_f32 v[38:39], v[154:155], v[84:85], v[38:39] op_sel_hi:[1,0,1]
	v_pk_fma_f32 v[8:9], v[156:157], v[84:85], v[8:9] op_sel_hi:[1,0,1]
	v_pk_fma_f32 v[28:29], v[156:157], v[86:87], v[28:29] op_sel_hi:[1,0,1]
	v_pk_fma_f32 v[30:31], v[154:155], v[86:87], v[30:31] op_sel_hi:[1,0,1]
	v_pk_fma_f32 v[2:3], v[156:157], v[86:87], v[2:3] op_sel:[0,1,0]
	v_pk_fma_f32 v[26:27], v[154:155], v[86:87], v[26:27] op_sel:[0,1,0]
	v_pk_fma_f32 v[22:23], v[154:155], v[88:89], v[22:23] op_sel_hi:[1,0,1]
	v_pk_fma_f32 v[4:5], v[156:157], v[88:89], v[4:5] op_sel_hi:[1,0,1]
	v_pk_fma_f32 v[20:21], v[154:155], v[106:107], v[20:21] op_sel_hi:[1,0,1]
	v_pk_fma_f32 v[24:25], v[156:157], v[106:107], v[24:25] op_sel_hi:[1,0,1]
	v_pk_fma_f32 v[18:19], v[154:155], v[108:109], v[18:19] op_sel_hi:[1,0,1]
	v_pk_fma_f32 v[16:17], v[156:157], v[108:109], v[16:17] op_sel_hi:[1,0,1]
	v_pk_fma_f32 v[46:47], v[160:161], v[90:91], v[32:33] op_sel_hi:[1,0,1]
	v_pk_fma_f32 v[48:49], v[158:159], v[90:91], v[34:35] op_sel_hi:[1,0,1]
	v_pk_fma_f32 v[40:41], v[160:161], v[90:91], v[6:7] op_sel:[0,1,0]
	v_pk_fma_f32 v[44:45], v[158:159], v[90:91], v[36:37] op_sel:[0,1,0]
	v_pk_fma_f32 v[36:37], v[160:161], v[92:93], v[8:9] op_sel_hi:[1,0,1]
	v_pk_fma_f32 v[38:39], v[158:159], v[92:93], v[38:39] op_sel_hi:[1,0,1]
	v_pk_fma_f32 v[32:33], v[160:161], v[110:111], v[24:25] op_sel_hi:[1,0,1]
	v_pk_fma_f32 v[34:35], v[158:159], v[110:111], v[20:21] op_sel_hi:[1,0,1]
	v_pk_fma_f32 v[28:29], v[160:161], v[94:95], v[28:29] op_sel_hi:[1,0,1]
	v_pk_fma_f32 v[30:31], v[158:159], v[94:95], v[30:31] op_sel_hi:[1,0,1]
	v_pk_fma_f32 v[24:25], v[160:161], v[94:95], v[2:3] op_sel:[0,1,0]
	v_pk_fma_f32 v[26:27], v[158:159], v[94:95], v[26:27] op_sel:[0,1,0]
	v_pk_fma_f32 v[20:21], v[160:161], v[96:97], v[4:5] op_sel_hi:[1,0,1]
	v_pk_fma_f32 v[22:23], v[158:159], v[96:97], v[22:23] op_sel_hi:[1,0,1]
	v_pk_fma_f32 v[16:17], v[160:161], v[112:113], v[16:17] op_sel_hi:[1,0,1]
	v_pk_fma_f32 v[18:19], v[158:159], v[112:113], v[18:19] op_sel_hi:[1,0,1]
	ds_read_b128 v[6:9], v50
	ds_read_b128 v[2:5], v50 offset:16
	ds_read_b128 v[52:55], v50 offset:256
	ds_read_b128 v[78:81], v50 offset:272
	ds_read_b128 v[82:85], v50 offset:512
	ds_read_b128 v[86:89], v50 offset:528
	ds_read_b128 v[90:93], v50 offset:768
	ds_read_b128 v[94:97], v50 offset:784
	s_waitcnt lgkmcnt(0)
	v_mov_b32_e32 v98, v9
	v_mov_b32_e32 v100, v5
	v_mov_b32_e32 v102, v55
	v_mov_b32_e32 v104, v81
	v_mov_b32_e32 v106, v85
	v_mov_b32_e32 v108, v89
	s_add_i32 s12, s12, 32
	v_mov_b32_e32 v110, v93
	v_mov_b32_e32 v112, v97
	v_add_u32_e32 v50, 0x400, v50
	s_cmpk_lg_i32 s12, 0x100
	s_waitcnt vmcnt(16)
; __device__ __forceinline__ void p0_ada(Frame& F, const float* c, const float* ada_w, const float* ada_b, float* mod) {
;     ...
;         for (int it = 0; it < 32; ++it) {
;             const int k = kbase + 8 * it;
;             const f32x4 w = __builtin_nontemporal_load((const f32x4*)(W + (size_t)k * 6 * D));
;             const f32x4 c0 = *(const f32x4*)(cond + k * 8), c1 = *(const f32x4*)(cond + k * 8 + 4);
;             acc[0] += w * c0[0]; acc[1] += w * c0[1]; acc[2] += w * c0[2]; acc[3] += w * c0[3];
;             acc[4] += w * c1[0]; acc[5] += w * c1[1]; acc[6] += w * c1[2]; acc[7] += w * c1[3];
;         }
	v_pk_fma_f32 v[48:49], v[162:163], v[6:7], v[48:49] op_sel_hi:[1,0,1]
	v_pk_fma_f32 v[46:47], v[164:165], v[6:7], v[46:47] op_sel_hi:[1,0,1]
	v_pk_fma_f32 v[44:45], v[162:163], v[6:7], v[44:45] op_sel:[0,1,0]
	v_pk_fma_f32 v[6:7], v[164:165], v[6:7], v[40:41] op_sel:[0,1,0]
	v_pk_fma_f32 v[38:39], v[162:163], v[8:9], v[38:39] op_sel_hi:[1,0,1]
	v_pk_fma_f32 v[8:9], v[164:165], v[8:9], v[36:37] op_sel_hi:[1,0,1]
	v_pk_fma_f32 v[30:31], v[162:163], v[2:3], v[30:31] op_sel_hi:[1,0,1]
	v_pk_fma_f32 v[28:29], v[164:165], v[2:3], v[28:29] op_sel_hi:[1,0,1]
	v_pk_fma_f32 v[26:27], v[162:163], v[2:3], v[26:27] op_sel:[0,1,0]
	v_pk_fma_f32 v[2:3], v[164:165], v[2:3], v[24:25] op_sel:[0,1,0]
	v_pk_fma_f32 v[22:23], v[162:163], v[4:5], v[22:23] op_sel_hi:[1,0,1]
	v_pk_fma_f32 v[4:5], v[164:165], v[4:5], v[20:21] op_sel_hi:[1,0,1]
	v_pk_fma_f32 v[20:21], v[162:163], v[98:99], v[34:35] op_sel_hi:[1,0,1]
	v_pk_fma_f32 v[24:25], v[164:165], v[98:99], v[32:33] op_sel_hi:[1,0,1]
	v_pk_fma_f32 v[18:19], v[162:163], v[100:101], v[18:19] op_sel_hi:[1,0,1]
	v_pk_fma_f32 v[16:17], v[164:165], v[100:101], v[16:17] op_sel_hi:[1,0,1]
	v_pk_fma_f32 v[32:33], v[168:169], v[52:53], v[46:47] op_sel_hi:[1,0,1]
	v_pk_fma_f32 v[34:35], v[166:167], v[52:53], v[48:49] op_sel_hi:[1,0,1]
	v_pk_fma_f32 v[6:7], v[168:169], v[52:53], v[6:7] op_sel:[0,1,0]
	v_pk_fma_f32 v[36:37], v[166:167], v[52:53], v[44:45] op_sel:[0,1,0]
	v_pk_fma_f32 v[8:9], v[168:169], v[54:55], v[8:9] op_sel_hi:[1,0,1]
	v_pk_fma_f32 v[38:39], v[166:167], v[54:55], v[38:39] op_sel_hi:[1,0,1]
	v_pk_fma_f32 v[28:29], v[168:169], v[78:79], v[28:29] op_sel_hi:[1,0,1]
	v_pk_fma_f32 v[30:31], v[166:167], v[78:79], v[30:31] op_sel_hi:[1,0,1]
	v_pk_fma_f32 v[2:3], v[168:169], v[78:79], v[2:3] op_sel:[0,1,0]
	v_pk_fma_f32 v[26:27], v[166:167], v[78:79], v[26:27] op_sel:[0,1,0]
	v_pk_fma_f32 v[4:5], v[168:169], v[80:81], v[4:5] op_sel_hi:[1,0,1]
	v_pk_fma_f32 v[22:23], v[166:167], v[80:81], v[22:23] op_sel_hi:[1,0,1]
	v_pk_fma_f32 v[24:25], v[168:169], v[102:103], v[24:25] op_sel_hi:[1,0,1]
	v_pk_fma_f32 v[20:21], v[166:167], v[102:103], v[20:21] op_sel_hi:[1,0,1]
	v_pk_fma_f32 v[16:17], v[168:169], v[104:105], v[16:17] op_sel_hi:[1,0,1]
	v_pk_fma_f32 v[18:19], v[166:167], v[104:105], v[18:19] op_sel_hi:[1,0,1]
	v_pk_fma_f32 v[32:33], v[172:173], v[82:83], v[32:33] op_sel_hi:[1,0,1]
	v_pk_fma_f32 v[34:35], v[170:171], v[82:83], v[34:35] op_sel_hi:[1,0,1]
	v_pk_fma_f32 v[6:7], v[172:173], v[82:83], v[6:7] op_sel:[0,1,0]
	v_pk_fma_f32 v[36:37], v[170:171], v[82:83], v[36:37] op_sel:[0,1,0]
	v_pk_fma_f32 v[38:39], v[170:171], v[84:85], v[38:39] op_sel_hi:[1,0,1]
	v_pk_fma_f32 v[8:9], v[172:173], v[84:85], v[8:9] op_sel_hi:[1,0,1]
	v_pk_fma_f32 v[28:29], v[172:173], v[86:87], v[28:29] op_sel_hi:[1,0,1]
	v_pk_fma_f32 v[30:31], v[170:171], v[86:87], v[30:31] op_sel_hi:[1,0,1]
	v_pk_fma_f32 v[2:3], v[172:173], v[86:87], v[2:3] op_sel:[0,1,0]
	v_pk_fma_f32 v[26:27], v[170:171], v[86:87], v[26:27] op_sel:[0,1,0]
	v_pk_fma_f32 v[22:23], v[170:171], v[88:89], v[22:23] op_sel_hi:[1,0,1]
	v_pk_fma_f32 v[4:5], v[172:173], v[88:89], v[4:5] op_sel_hi:[1,0,1]
	v_pk_fma_f32 v[20:21], v[170:171], v[106:107], v[20:21] op_sel_hi:[1,0,1]
	v_pk_fma_f32 v[24:25], v[172:173], v[106:107], v[24:25] op_sel_hi:[1,0,1]
	v_pk_fma_f32 v[18:19], v[170:171], v[108:109], v[18:19] op_sel_hi:[1,0,1]
	v_pk_fma_f32 v[16:17], v[172:173], v[108:109], v[16:17] op_sel_hi:[1,0,1]
	v_pk_fma_f32 v[46:47], v[176:177], v[90:91], v[32:33] op_sel_hi:[1,0,1]
	v_pk_fma_f32 v[48:49], v[174:175], v[90:91], v[34:35] op_sel_hi:[1,0,1]
	v_pk_fma_f32 v[40:41], v[176:177], v[90:91], v[6:7] op_sel:[0,1,0]
	v_pk_fma_f32 v[44:45], v[174:175], v[90:91], v[36:37] op_sel:[0,1,0]
	v_pk_fma_f32 v[36:37], v[176:177], v[92:93], v[8:9] op_sel_hi:[1,0,1]
	v_pk_fma_f32 v[38:39], v[174:175], v[92:93], v[38:39] op_sel_hi:[1,0,1]
	v_pk_fma_f32 v[32:33], v[176:177], v[110:111], v[24:25] op_sel_hi:[1,0,1]
	v_pk_fma_f32 v[34:35], v[174:175], v[110:111], v[20:21] op_sel_hi:[1,0,1]
	v_pk_fma_f32 v[28:29], v[176:177], v[94:95], v[28:29] op_sel_hi:[1,0,1]
	v_pk_fma_f32 v[30:31], v[174:175], v[94:95], v[30:31] op_sel_hi:[1,0,1]
	v_pk_fma_f32 v[24:25], v[176:177], v[94:95], v[2:3] op_sel:[0,1,0]
	v_pk_fma_f32 v[26:27], v[174:175], v[94:95], v[26:27] op_sel:[0,1,0]
	v_pk_fma_f32 v[20:21], v[176:177], v[96:97], v[4:5] op_sel_hi:[1,0,1]
	v_pk_fma_f32 v[22:23], v[174:175], v[96:97], v[22:23] op_sel_hi:[1,0,1]
	v_pk_fma_f32 v[16:17], v[176:177], v[112:113], v[16:17] op_sel_hi:[1,0,1]
	v_pk_fma_f32 v[18:19], v[174:175], v[112:113], v[18:19] op_sel_hi:[1,0,1]
	ds_read_b128 v[6:9], v50
	ds_read_b128 v[2:5], v50 offset:16
	ds_read_b128 v[52:55], v50 offset:256
	ds_read_b128 v[78:81], v50 offset:272
	ds_read_b128 v[82:85], v50 offset:512
	ds_read_b128 v[86:89], v50 offset:528
	ds_read_b128 v[90:93], v50 offset:768
	ds_read_b128 v[94:97], v50 offset:784
	s_waitcnt lgkmcnt(0)
	v_mov_b32_e32 v98, v9
	v_mov_b32_e32 v100, v5
	v_mov_b32_e32 v102, v55
	v_mov_b32_e32 v104, v81
	v_mov_b32_e32 v106, v85
	v_mov_b32_e32 v108, v89
	s_add_i32 s12, s12, 32
	v_mov_b32_e32 v110, v93
	v_mov_b32_e32 v112, v97
	v_add_u32_e32 v50, 0x400, v50
	s_cmpk_lg_i32 s12, 0x100
	s_waitcnt vmcnt(12)
; __device__ __forceinline__ void p0_ada(Frame& F, const float* c, const float* ada_w, const float* ada_b, float* mod) {
;     ...
;         for (int it = 0; it < 32; ++it) {
;             const int k = kbase + 8 * it;
;             const f32x4 w = __builtin_nontemporal_load((const f32x4*)(W + (size_t)k * 6 * D));
;             const f32x4 c0 = *(const f32x4*)(cond + k * 8), c1 = *(const f32x4*)(cond + k * 8 + 4);
;             acc[0] += w * c0[0]; acc[1] += w * c0[1]; acc[2] += w * c0[2]; acc[3] += w * c0[3];
;             acc[4] += w * c1[0]; acc[5] += w * c1[1]; acc[6] += w * c1[2]; acc[7] += w * c1[3];
;         }
	v_pk_fma_f32 v[48:49], v[178:179], v[6:7], v[48:49] op_sel_hi:[1,0,1]
	v_pk_fma_f32 v[46:47], v[180:181], v[6:7], v[46:47] op_sel_hi:[1,0,1]
	v_pk_fma_f32 v[44:45], v[178:179], v[6:7], v[44:45] op_sel:[0,1,0]
	v_pk_fma_f32 v[6:7], v[180:181], v[6:7], v[40:41] op_sel:[0,1,0]
	v_pk_fma_f32 v[38:39], v[178:179], v[8:9], v[38:39] op_sel_hi:[1,0,1]
	v_pk_fma_f32 v[8:9], v[180:181], v[8:9], v[36:37] op_sel_hi:[1,0,1]
	v_pk_fma_f32 v[30:31], v[178:179], v[2:3], v[30:31] op_sel_hi:[1,0,1]
	v_pk_fma_f32 v[28:29], v[180:181], v[2:3], v[28:29] op_sel_hi:[1,0,1]
	v_pk_fma_f32 v[26:27], v[178:179], v[2:3], v[26:27] op_sel:[0,1,0]
	v_pk_fma_f32 v[2:3], v[180:181], v[2:3], v[24:25] op_sel:[0,1,0]
	v_pk_fma_f32 v[22:23], v[178:179], v[4:5], v[22:23] op_sel_hi:[1,0,1]
	v_pk_fma_f32 v[4:5], v[180:181], v[4:5], v[20:21] op_sel_hi:[1,0,1]
	v_pk_fma_f32 v[20:21], v[178:179], v[98:99], v[34:35] op_sel_hi:[1,0,1]
	v_pk_fma_f32 v[24:25], v[180:181], v[98:99], v[32:33] op_sel_hi:[1,0,1]
	v_pk_fma_f32 v[18:19], v[178:179], v[100:101], v[18:19] op_sel_hi:[1,0,1]
	v_pk_fma_f32 v[16:17], v[180:181], v[100:101], v[16:17] op_sel_hi:[1,0,1]
	v_pk_fma_f32 v[32:33], v[184:185], v[52:53], v[46:47] op_sel_hi:[1,0,1]
	v_pk_fma_f32 v[34:35], v[182:183], v[52:53], v[48:49] op_sel_hi:[1,0,1]
	v_pk_fma_f32 v[6:7], v[184:185], v[52:53], v[6:7] op_sel:[0,1,0]
	v_pk_fma_f32 v[36:37], v[182:183], v[52:53], v[44:45] op_sel:[0,1,0]
	v_pk_fma_f32 v[8:9], v[184:185], v[54:55], v[8:9] op_sel_hi:[1,0,1]
	v_pk_fma_f32 v[38:39], v[182:183], v[54:55], v[38:39] op_sel_hi:[1,0,1]
	v_pk_fma_f32 v[28:29], v[184:185], v[78:79], v[28:29] op_sel_hi:[1,0,1]
	v_pk_fma_f32 v[30:31], v[182:183], v[78:79], v[30:31] op_sel_hi:[1,0,1]
	v_pk_fma_f32 v[2:3], v[184:185], v[78:79], v[2:3] op_sel:[0,1,0]
	v_pk_fma_f32 v[26:27], v[182:183], v[78:79], v[26:27] op_sel:[0,1,0]
	v_pk_fma_f32 v[4:5], v[184:185], v[80:81], v[4:5] op_sel_hi:[1,0,1]
	v_pk_fma_f32 v[22:23], v[182:183], v[80:81], v[22:23] op_sel_hi:[1,0,1]
	v_pk_fma_f32 v[24:25], v[184:185], v[102:103], v[24:25] op_sel_hi:[1,0,1]
	v_pk_fma_f32 v[20:21], v[182:183], v[102:103], v[20:21] op_sel_hi:[1,0,1]
	v_pk_fma_f32 v[16:17], v[184:185], v[104:105], v[16:17] op_sel_hi:[1,0,1]
	v_pk_fma_f32 v[18:19], v[182:183], v[104:105], v[18:19] op_sel_hi:[1,0,1]
	v_pk_fma_f32 v[32:33], v[188:189], v[82:83], v[32:33] op_sel_hi:[1,0,1]
	v_pk_fma_f32 v[34:35], v[186:187], v[82:83], v[34:35] op_sel_hi:[1,0,1]
	v_pk_fma_f32 v[6:7], v[188:189], v[82:83], v[6:7] op_sel:[0,1,0]
	v_pk_fma_f32 v[36:37], v[186:187], v[82:83], v[36:37] op_sel:[0,1,0]
	v_pk_fma_f32 v[38:39], v[186:187], v[84:85], v[38:39] op_sel_hi:[1,0,1]
	v_pk_fma_f32 v[8:9], v[188:189], v[84:85], v[8:9] op_sel_hi:[1,0,1]
	v_pk_fma_f32 v[28:29], v[188:189], v[86:87], v[28:29] op_sel_hi:[1,0,1]
	v_pk_fma_f32 v[30:31], v[186:187], v[86:87], v[30:31] op_sel_hi:[1,0,1]
	v_pk_fma_f32 v[2:3], v[188:189], v[86:87], v[2:3] op_sel:[0,1,0]
	v_pk_fma_f32 v[26:27], v[186:187], v[86:87], v[26:27] op_sel:[0,1,0]
	v_pk_fma_f32 v[22:23], v[186:187], v[88:89], v[22:23] op_sel_hi:[1,0,1]
	v_pk_fma_f32 v[4:5], v[188:189], v[88:89], v[4:5] op_sel_hi:[1,0,1]
	v_pk_fma_f32 v[20:21], v[186:187], v[106:107], v[20:21] op_sel_hi:[1,0,1]
	v_pk_fma_f32 v[24:25], v[188:189], v[106:107], v[24:25] op_sel_hi:[1,0,1]
	v_pk_fma_f32 v[18:19], v[186:187], v[108:109], v[18:19] op_sel_hi:[1,0,1]
	v_pk_fma_f32 v[16:17], v[188:189], v[108:109], v[16:17] op_sel_hi:[1,0,1]
	v_pk_fma_f32 v[46:47], v[192:193], v[90:91], v[32:33] op_sel_hi:[1,0,1]
	v_pk_fma_f32 v[48:49], v[190:191], v[90:91], v[34:35] op_sel_hi:[1,0,1]
	v_pk_fma_f32 v[40:41], v[192:193], v[90:91], v[6:7] op_sel:[0,1,0]
	v_pk_fma_f32 v[44:45], v[190:191], v[90:91], v[36:37] op_sel:[0,1,0]
	v_pk_fma_f32 v[36:37], v[192:193], v[92:93], v[8:9] op_sel_hi:[1,0,1]
	v_pk_fma_f32 v[38:39], v[190:191], v[92:93], v[38:39] op_sel_hi:[1,0,1]
	v_pk_fma_f32 v[32:33], v[192:193], v[110:111], v[24:25] op_sel_hi:[1,0,1]
	v_pk_fma_f32 v[34:35], v[190:191], v[110:111], v[20:21] op_sel_hi:[1,0,1]
	v_pk_fma_f32 v[28:29], v[192:193], v[94:95], v[28:29] op_sel_hi:[1,0,1]
	v_pk_fma_f32 v[30:31], v[190:191], v[94:95], v[30:31] op_sel_hi:[1,0,1]
	v_pk_fma_f32 v[24:25], v[192:193], v[94:95], v[2:3] op_sel:[0,1,0]
	v_pk_fma_f32 v[26:27], v[190:191], v[94:95], v[26:27] op_sel:[0,1,0]
	v_pk_fma_f32 v[20:21], v[192:193], v[96:97], v[4:5] op_sel_hi:[1,0,1]
	v_pk_fma_f32 v[22:23], v[190:191], v[96:97], v[22:23] op_sel_hi:[1,0,1]
	v_pk_fma_f32 v[16:17], v[192:193], v[112:113], v[16:17] op_sel_hi:[1,0,1]
	v_pk_fma_f32 v[18:19], v[190:191], v[112:113], v[18:19] op_sel_hi:[1,0,1]
	ds_read_b128 v[6:9], v50
	ds_read_b128 v[2:5], v50 offset:16
	ds_read_b128 v[52:55], v50 offset:256
	ds_read_b128 v[78:81], v50 offset:272
	ds_read_b128 v[82:85], v50 offset:512
	ds_read_b128 v[86:89], v50 offset:528
	ds_read_b128 v[90:93], v50 offset:768
	ds_read_b128 v[94:97], v50 offset:784
	s_waitcnt lgkmcnt(0)
	v_mov_b32_e32 v98, v9
	v_mov_b32_e32 v100, v5
	v_mov_b32_e32 v102, v55
	v_mov_b32_e32 v104, v81
	v_mov_b32_e32 v106, v85
	v_mov_b32_e32 v108, v89
	s_add_i32 s12, s12, 32
	v_mov_b32_e32 v110, v93
	v_mov_b32_e32 v112, v97
	v_add_u32_e32 v50, 0x400, v50
	s_cmpk_lg_i32 s12, 0x100
	s_waitcnt vmcnt(8)
; __device__ __forceinline__ void p0_ada(Frame& F, const float* c, const float* ada_w, const float* ada_b, float* mod) {
;     ...
;         for (int it = 0; it < 32; ++it) {
;             const int k = kbase + 8 * it;
;             const f32x4 w = __builtin_nontemporal_load((const f32x4*)(W + (size_t)k * 6 * D));
;             const f32x4 c0 = *(const f32x4*)(cond + k * 8), c1 = *(const f32x4*)(cond + k * 8 + 4);
;             acc[0] += w * c0[0]; acc[1] += w * c0[1]; acc[2] += w * c0[2]; acc[3] += w * c0[3];
;             acc[4] += w * c1[0]; acc[5] += w * c1[1]; acc[6] += w * c1[2]; acc[7] += w * c1[3];
;         }
	v_pk_fma_f32 v[48:49], v[196:197], v[6:7], v[48:49] op_sel_hi:[1,0,1]
	v_pk_fma_f32 v[46:47], v[198:199], v[6:7], v[46:47] op_sel_hi:[1,0,1]
	v_pk_fma_f32 v[44:45], v[196:197], v[6:7], v[44:45] op_sel:[0,1,0]
	v_pk_fma_f32 v[6:7], v[198:199], v[6:7], v[40:41] op_sel:[0,1,0]
	v_pk_fma_f32 v[38:39], v[196:197], v[8:9], v[38:39] op_sel_hi:[1,0,1]
	v_pk_fma_f32 v[8:9], v[198:199], v[8:9], v[36:37] op_sel_hi:[1,0,1]
	v_pk_fma_f32 v[30:31], v[196:197], v[2:3], v[30:31] op_sel_hi:[1,0,1]
	v_pk_fma_f32 v[28:29], v[198:199], v[2:3], v[28:29] op_sel_hi:[1,0,1]
	v_pk_fma_f32 v[26:27], v[196:197], v[2:3], v[26:27] op_sel:[0,1,0]
	v_pk_fma_f32 v[2:3], v[198:199], v[2:3], v[24:25] op_sel:[0,1,0]
	v_pk_fma_f32 v[22:23], v[196:197], v[4:5], v[22:23] op_sel_hi:[1,0,1]
	v_pk_fma_f32 v[4:5], v[198:199], v[4:5], v[20:21] op_sel_hi:[1,0,1]
	v_pk_fma_f32 v[20:21], v[196:197], v[98:99], v[34:35] op_sel_hi:[1,0,1]
	v_pk_fma_f32 v[24:25], v[198:199], v[98:99], v[32:33] op_sel_hi:[1,0,1]
	v_pk_fma_f32 v[18:19], v[196:197], v[100:101], v[18:19] op_sel_hi:[1,0,1]
	v_pk_fma_f32 v[16:17], v[198:199], v[100:101], v[16:17] op_sel_hi:[1,0,1]
	v_pk_fma_f32 v[32:33], v[202:203], v[52:53], v[46:47] op_sel_hi:[1,0,1]
	v_pk_fma_f32 v[34:35], v[200:201], v[52:53], v[48:49] op_sel_hi:[1,0,1]
	v_pk_fma_f32 v[6:7], v[202:203], v[52:53], v[6:7] op_sel:[0,1,0]
	v_pk_fma_f32 v[36:37], v[200:201], v[52:53], v[44:45] op_sel:[0,1,0]
	v_pk_fma_f32 v[8:9], v[202:203], v[54:55], v[8:9] op_sel_hi:[1,0,1]
	v_pk_fma_f32 v[38:39], v[200:201], v[54:55], v[38:39] op_sel_hi:[1,0,1]
	v_pk_fma_f32 v[28:29], v[202:203], v[78:79], v[28:29] op_sel_hi:[1,0,1]
	v_pk_fma_f32 v[30:31], v[200:201], v[78:79], v[30:31] op_sel_hi:[1,0,1]
	v_pk_fma_f32 v[2:3], v[202:203], v[78:79], v[2:3] op_sel:[0,1,0]
	v_pk_fma_f32 v[26:27], v[200:201], v[78:79], v[26:27] op_sel:[0,1,0]
	v_pk_fma_f32 v[4:5], v[202:203], v[80:81], v[4:5] op_sel_hi:[1,0,1]
	v_pk_fma_f32 v[22:23], v[200:201], v[80:81], v[22:23] op_sel_hi:[1,0,1]
	v_pk_fma_f32 v[24:25], v[202:203], v[102:103], v[24:25] op_sel_hi:[1,0,1]
	v_pk_fma_f32 v[20:21], v[200:201], v[102:103], v[20:21] op_sel_hi:[1,0,1]
	v_pk_fma_f32 v[16:17], v[202:203], v[104:105], v[16:17] op_sel_hi:[1,0,1]
	v_pk_fma_f32 v[18:19], v[200:201], v[104:105], v[18:19] op_sel_hi:[1,0,1]
	v_pk_fma_f32 v[32:33], v[206:207], v[82:83], v[32:33] op_sel_hi:[1,0,1]
	v_pk_fma_f32 v[34:35], v[204:205], v[82:83], v[34:35] op_sel_hi:[1,0,1]
	v_pk_fma_f32 v[6:7], v[206:207], v[82:83], v[6:7] op_sel:[0,1,0]
	v_pk_fma_f32 v[36:37], v[204:205], v[82:83], v[36:37] op_sel:[0,1,0]
	v_pk_fma_f32 v[38:39], v[204:205], v[84:85], v[38:39] op_sel_hi:[1,0,1]
	v_pk_fma_f32 v[8:9], v[206:207], v[84:85], v[8:9] op_sel_hi:[1,0,1]
	v_pk_fma_f32 v[28:29], v[206:207], v[86:87], v[28:29] op_sel_hi:[1,0,1]
	v_pk_fma_f32 v[30:31], v[204:205], v[86:87], v[30:31] op_sel_hi:[1,0,1]
	v_pk_fma_f32 v[2:3], v[206:207], v[86:87], v[2:3] op_sel:[0,1,0]
	v_pk_fma_f32 v[26:27], v[204:205], v[86:87], v[26:27] op_sel:[0,1,0]
	v_pk_fma_f32 v[22:23], v[204:205], v[88:89], v[22:23] op_sel_hi:[1,0,1]
	v_pk_fma_f32 v[4:5], v[206:207], v[88:89], v[4:5] op_sel_hi:[1,0,1]
	v_pk_fma_f32 v[20:21], v[204:205], v[106:107], v[20:21] op_sel_hi:[1,0,1]
	v_pk_fma_f32 v[24:25], v[206:207], v[106:107], v[24:25] op_sel_hi:[1,0,1]
	v_pk_fma_f32 v[18:19], v[204:205], v[108:109], v[18:19] op_sel_hi:[1,0,1]
	v_pk_fma_f32 v[16:17], v[206:207], v[108:109], v[16:17] op_sel_hi:[1,0,1]
	v_pk_fma_f32 v[46:47], v[210:211], v[90:91], v[32:33] op_sel_hi:[1,0,1]
	v_pk_fma_f32 v[48:49], v[208:209], v[90:91], v[34:35] op_sel_hi:[1,0,1]
	v_pk_fma_f32 v[40:41], v[210:211], v[90:91], v[6:7] op_sel:[0,1,0]
	v_pk_fma_f32 v[44:45], v[208:209], v[90:91], v[36:37] op_sel:[0,1,0]
	v_pk_fma_f32 v[36:37], v[210:211], v[92:93], v[8:9] op_sel_hi:[1,0,1]
	v_pk_fma_f32 v[38:39], v[208:209], v[92:93], v[38:39] op_sel_hi:[1,0,1]
	v_pk_fma_f32 v[32:33], v[210:211], v[110:111], v[24:25] op_sel_hi:[1,0,1]
	v_pk_fma_f32 v[34:35], v[208:209], v[110:111], v[20:21] op_sel_hi:[1,0,1]
	v_pk_fma_f32 v[28:29], v[210:211], v[94:95], v[28:29] op_sel_hi:[1,0,1]
	v_pk_fma_f32 v[30:31], v[208:209], v[94:95], v[30:31] op_sel_hi:[1,0,1]
	v_pk_fma_f32 v[24:25], v[210:211], v[94:95], v[2:3] op_sel:[0,1,0]
	v_pk_fma_f32 v[26:27], v[208:209], v[94:95], v[26:27] op_sel:[0,1,0]
	v_pk_fma_f32 v[20:21], v[210:211], v[96:97], v[4:5] op_sel_hi:[1,0,1]
	v_pk_fma_f32 v[22:23], v[208:209], v[96:97], v[22:23] op_sel_hi:[1,0,1]
	v_pk_fma_f32 v[16:17], v[210:211], v[112:113], v[16:17] op_sel_hi:[1,0,1]
	v_pk_fma_f32 v[18:19], v[208:209], v[112:113], v[18:19] op_sel_hi:[1,0,1]
	ds_read_b128 v[6:9], v50
	ds_read_b128 v[2:5], v50 offset:16
	ds_read_b128 v[52:55], v50 offset:256
	ds_read_b128 v[78:81], v50 offset:272
	ds_read_b128 v[82:85], v50 offset:512
	ds_read_b128 v[86:89], v50 offset:528
	ds_read_b128 v[90:93], v50 offset:768
	ds_read_b128 v[94:97], v50 offset:784
	s_waitcnt lgkmcnt(0)
	v_mov_b32_e32 v98, v9
	v_mov_b32_e32 v100, v5
	v_mov_b32_e32 v102, v55
	v_mov_b32_e32 v104, v81
	v_mov_b32_e32 v106, v85
	v_mov_b32_e32 v108, v89
	s_add_i32 s12, s12, 32
	v_mov_b32_e32 v110, v93
	v_mov_b32_e32 v112, v97
	v_add_u32_e32 v50, 0x400, v50
	s_cmpk_lg_i32 s12, 0x100
	s_waitcnt vmcnt(4)
; __device__ __forceinline__ void p0_ada(Frame& F, const float* c, const float* ada_w, const float* ada_b, float* mod) {
;     ...
;         for (int it = 0; it < 32; ++it) {
;             const int k = kbase + 8 * it;
;             const f32x4 w = __builtin_nontemporal_load((const f32x4*)(W + (size_t)k * 6 * D));
;             const f32x4 c0 = *(const f32x4*)(cond + k * 8), c1 = *(const f32x4*)(cond + k * 8 + 4);
;             acc[0] += w * c0[0]; acc[1] += w * c0[1]; acc[2] += w * c0[2]; acc[3] += w * c0[3];
;             acc[4] += w * c1[0]; acc[5] += w * c1[1]; acc[6] += w * c1[2]; acc[7] += w * c1[3];
;         }
	v_pk_fma_f32 v[48:49], v[212:213], v[6:7], v[48:49] op_sel_hi:[1,0,1]
	v_pk_fma_f32 v[46:47], v[214:215], v[6:7], v[46:47] op_sel_hi:[1,0,1]
	v_pk_fma_f32 v[44:45], v[212:213], v[6:7], v[44:45] op_sel:[0,1,0]
	v_pk_fma_f32 v[6:7], v[214:215], v[6:7], v[40:41] op_sel:[0,1,0]
	v_pk_fma_f32 v[38:39], v[212:213], v[8:9], v[38:39] op_sel_hi:[1,0,1]
	v_pk_fma_f32 v[8:9], v[214:215], v[8:9], v[36:37] op_sel_hi:[1,0,1]
	v_pk_fma_f32 v[30:31], v[212:213], v[2:3], v[30:31] op_sel_hi:[1,0,1]
	v_pk_fma_f32 v[28:29], v[214:215], v[2:3], v[28:29] op_sel_hi:[1,0,1]
	v_pk_fma_f32 v[26:27], v[212:213], v[2:3], v[26:27] op_sel:[0,1,0]
	v_pk_fma_f32 v[2:3], v[214:215], v[2:3], v[24:25] op_sel:[0,1,0]
	v_pk_fma_f32 v[22:23], v[212:213], v[4:5], v[22:23] op_sel_hi:[1,0,1]
	v_pk_fma_f32 v[4:5], v[214:215], v[4:5], v[20:21] op_sel_hi:[1,0,1]
	v_pk_fma_f32 v[20:21], v[212:213], v[98:99], v[34:35] op_sel_hi:[1,0,1]
	v_pk_fma_f32 v[24:25], v[214:215], v[98:99], v[32:33] op_sel_hi:[1,0,1]
	v_pk_fma_f32 v[18:19], v[212:213], v[100:101], v[18:19] op_sel_hi:[1,0,1]
	v_pk_fma_f32 v[16:17], v[214:215], v[100:101], v[16:17] op_sel_hi:[1,0,1]
	v_pk_fma_f32 v[32:33], v[218:219], v[52:53], v[46:47] op_sel_hi:[1,0,1]
	v_pk_fma_f32 v[34:35], v[216:217], v[52:53], v[48:49] op_sel_hi:[1,0,1]
	v_pk_fma_f32 v[6:7], v[218:219], v[52:53], v[6:7] op_sel:[0,1,0]
	v_pk_fma_f32 v[36:37], v[216:217], v[52:53], v[44:45] op_sel:[0,1,0]
	v_pk_fma_f32 v[8:9], v[218:219], v[54:55], v[8:9] op_sel_hi:[1,0,1]
	v_pk_fma_f32 v[38:39], v[216:217], v[54:55], v[38:39] op_sel_hi:[1,0,1]
	v_pk_fma_f32 v[28:29], v[218:219], v[78:79], v[28:29] op_sel_hi:[1,0,1]
	v_pk_fma_f32 v[30:31], v[216:217], v[78:79], v[30:31] op_sel_hi:[1,0,1]
	v_pk_fma_f32 v[2:3], v[218:219], v[78:79], v[2:3] op_sel:[0,1,0]
	v_pk_fma_f32 v[26:27], v[216:217], v[78:79], v[26:27] op_sel:[0,1,0]
	v_pk_fma_f32 v[4:5], v[218:219], v[80:81], v[4:5] op_sel_hi:[1,0,1]
	v_pk_fma_f32 v[22:23], v[216:217], v[80:81], v[22:23] op_sel_hi:[1,0,1]
	v_pk_fma_f32 v[24:25], v[218:219], v[102:103], v[24:25] op_sel_hi:[1,0,1]
	v_pk_fma_f32 v[20:21], v[216:217], v[102:103], v[20:21] op_sel_hi:[1,0,1]
	v_pk_fma_f32 v[16:17], v[218:219], v[104:105], v[16:17] op_sel_hi:[1,0,1]
	v_pk_fma_f32 v[18:19], v[216:217], v[104:105], v[18:19] op_sel_hi:[1,0,1]
	v_pk_fma_f32 v[32:33], v[222:223], v[82:83], v[32:33] op_sel_hi:[1,0,1]
	v_pk_fma_f32 v[34:35], v[220:221], v[82:83], v[34:35] op_sel_hi:[1,0,1]
	v_pk_fma_f32 v[6:7], v[222:223], v[82:83], v[6:7] op_sel:[0,1,0]
	v_pk_fma_f32 v[36:37], v[220:221], v[82:83], v[36:37] op_sel:[0,1,0]
	v_pk_fma_f32 v[38:39], v[220:221], v[84:85], v[38:39] op_sel_hi:[1,0,1]
	v_pk_fma_f32 v[8:9], v[222:223], v[84:85], v[8:9] op_sel_hi:[1,0,1]
	v_pk_fma_f32 v[28:29], v[222:223], v[86:87], v[28:29] op_sel_hi:[1,0,1]
	v_pk_fma_f32 v[30:31], v[220:221], v[86:87], v[30:31] op_sel_hi:[1,0,1]
	v_pk_fma_f32 v[2:3], v[222:223], v[86:87], v[2:3] op_sel:[0,1,0]
	v_pk_fma_f32 v[26:27], v[220:221], v[86:87], v[26:27] op_sel:[0,1,0]
	v_pk_fma_f32 v[22:23], v[220:221], v[88:89], v[22:23] op_sel_hi:[1,0,1]
	v_pk_fma_f32 v[4:5], v[222:223], v[88:89], v[4:5] op_sel_hi:[1,0,1]
	v_pk_fma_f32 v[20:21], v[220:221], v[106:107], v[20:21] op_sel_hi:[1,0,1]
	v_pk_fma_f32 v[24:25], v[222:223], v[106:107], v[24:25] op_sel_hi:[1,0,1]
	v_pk_fma_f32 v[18:19], v[220:221], v[108:109], v[18:19] op_sel_hi:[1,0,1]
	v_pk_fma_f32 v[16:17], v[222:223], v[108:109], v[16:17] op_sel_hi:[1,0,1]
	v_pk_fma_f32 v[46:47], v[226:227], v[90:91], v[32:33] op_sel_hi:[1,0,1]
	v_pk_fma_f32 v[48:49], v[224:225], v[90:91], v[34:35] op_sel_hi:[1,0,1]
	v_pk_fma_f32 v[40:41], v[226:227], v[90:91], v[6:7] op_sel:[0,1,0]
	v_pk_fma_f32 v[44:45], v[224:225], v[90:91], v[36:37] op_sel:[0,1,0]
	v_pk_fma_f32 v[36:37], v[226:227], v[92:93], v[8:9] op_sel_hi:[1,0,1]
	v_pk_fma_f32 v[38:39], v[224:225], v[92:93], v[38:39] op_sel_hi:[1,0,1]
	v_pk_fma_f32 v[32:33], v[226:227], v[110:111], v[24:25] op_sel_hi:[1,0,1]
	v_pk_fma_f32 v[34:35], v[224:225], v[110:111], v[20:21] op_sel_hi:[1,0,1]
	v_pk_fma_f32 v[28:29], v[226:227], v[94:95], v[28:29] op_sel_hi:[1,0,1]
	v_pk_fma_f32 v[30:31], v[224:225], v[94:95], v[30:31] op_sel_hi:[1,0,1]
	v_pk_fma_f32 v[24:25], v[226:227], v[94:95], v[2:3] op_sel:[0,1,0]
	v_pk_fma_f32 v[26:27], v[224:225], v[94:95], v[26:27] op_sel:[0,1,0]
	v_pk_fma_f32 v[20:21], v[226:227], v[96:97], v[4:5] op_sel_hi:[1,0,1]
	v_pk_fma_f32 v[22:23], v[224:225], v[96:97], v[22:23] op_sel_hi:[1,0,1]
	v_pk_fma_f32 v[16:17], v[226:227], v[112:113], v[16:17] op_sel_hi:[1,0,1]
	v_pk_fma_f32 v[18:19], v[224:225], v[112:113], v[18:19] op_sel_hi:[1,0,1]
	ds_read_b128 v[6:9], v50
	ds_read_b128 v[2:5], v50 offset:16
	ds_read_b128 v[52:55], v50 offset:256
	ds_read_b128 v[78:81], v50 offset:272
	ds_read_b128 v[82:85], v50 offset:512
	ds_read_b128 v[86:89], v50 offset:528
	ds_read_b128 v[90:93], v50 offset:768
	ds_read_b128 v[94:97], v50 offset:784
	s_waitcnt lgkmcnt(0)
	v_mov_b32_e32 v98, v9
	v_mov_b32_e32 v100, v5
	v_mov_b32_e32 v102, v55
	v_mov_b32_e32 v104, v81
	v_mov_b32_e32 v106, v85
	v_mov_b32_e32 v108, v89
	s_add_i32 s12, s12, 32
	v_mov_b32_e32 v110, v93
	v_mov_b32_e32 v112, v97
	v_add_u32_e32 v50, 0x400, v50
	s_cmpk_lg_i32 s12, 0x100
	s_waitcnt vmcnt(0)
; __device__ __forceinline__ void p0_ada(Frame& F, const float* c, const float* ada_w, const float* ada_b, float* mod) {
;     ...
;         for (int it = 0; it < 32; ++it) {
;             const int k = kbase + 8 * it;
;             const f32x4 w = __builtin_nontemporal_load((const f32x4*)(W + (size_t)k * 6 * D));
;             const f32x4 c0 = *(const f32x4*)(cond + k * 8), c1 = *(const f32x4*)(cond + k * 8 + 4);
;             acc[0] += w * c0[0]; acc[1] += w * c0[1]; acc[2] += w * c0[2]; acc[3] += w * c0[3];
;             acc[4] += w * c1[0]; acc[5] += w * c1[1]; acc[6] += w * c1[2]; acc[7] += w * c1[3];
;         }
; #pragma unroll
;         for (int b = 0; b < 8; ++b)
; #pragma unroll
;             for (int j = 0; j < 4; ++j) { float v = acc[b][j]; v += __shfl_xor(v, 8); v += __shfl_xor(v, 16); v += __shfl_xor(v, 32); acc[b][j] = v; }
	v_pk_fma_f32 v[48:49], v[228:229], v[6:7], v[48:49] op_sel_hi:[1,0,1]
	v_pk_fma_f32 v[46:47], v[230:231], v[6:7], v[46:47] op_sel_hi:[1,0,1]
	v_pk_fma_f32 v[44:45], v[228:229], v[6:7], v[44:45] op_sel:[0,1,0]
	v_pk_fma_f32 v[6:7], v[230:231], v[6:7], v[40:41] op_sel:[0,1,0]
	v_pk_fma_f32 v[38:39], v[228:229], v[8:9], v[38:39] op_sel_hi:[1,0,1]
	v_pk_fma_f32 v[8:9], v[230:231], v[8:9], v[36:37] op_sel_hi:[1,0,1]
	v_pk_fma_f32 v[30:31], v[228:229], v[2:3], v[30:31] op_sel_hi:[1,0,1]
	v_pk_fma_f32 v[28:29], v[230:231], v[2:3], v[28:29] op_sel_hi:[1,0,1]
	v_pk_fma_f32 v[26:27], v[228:229], v[2:3], v[26:27] op_sel:[0,1,0]
	v_pk_fma_f32 v[2:3], v[230:231], v[2:3], v[24:25] op_sel:[0,1,0]
	v_pk_fma_f32 v[22:23], v[228:229], v[4:5], v[22:23] op_sel_hi:[1,0,1]
	v_pk_fma_f32 v[4:5], v[230:231], v[4:5], v[20:21] op_sel_hi:[1,0,1]
	v_pk_fma_f32 v[20:21], v[228:229], v[98:99], v[34:35] op_sel_hi:[1,0,1]
	v_pk_fma_f32 v[24:25], v[230:231], v[98:99], v[32:33] op_sel_hi:[1,0,1]
	v_pk_fma_f32 v[18:19], v[228:229], v[100:101], v[18:19] op_sel_hi:[1,0,1]
	v_pk_fma_f32 v[16:17], v[230:231], v[100:101], v[16:17] op_sel_hi:[1,0,1]
	v_pk_fma_f32 v[32:33], v[234:235], v[52:53], v[46:47] op_sel_hi:[1,0,1]
	v_pk_fma_f32 v[34:35], v[232:233], v[52:53], v[48:49] op_sel_hi:[1,0,1]
	v_pk_fma_f32 v[6:7], v[234:235], v[52:53], v[6:7] op_sel:[0,1,0]
	v_pk_fma_f32 v[36:37], v[232:233], v[52:53], v[44:45] op_sel:[0,1,0]
	v_pk_fma_f32 v[8:9], v[234:235], v[54:55], v[8:9] op_sel_hi:[1,0,1]
	v_pk_fma_f32 v[38:39], v[232:233], v[54:55], v[38:39] op_sel_hi:[1,0,1]
	v_pk_fma_f32 v[28:29], v[234:235], v[78:79], v[28:29] op_sel_hi:[1,0,1]
	v_pk_fma_f32 v[30:31], v[232:233], v[78:79], v[30:31] op_sel_hi:[1,0,1]
	v_pk_fma_f32 v[2:3], v[234:235], v[78:79], v[2:3] op_sel:[0,1,0]
	v_pk_fma_f32 v[26:27], v[232:233], v[78:79], v[26:27] op_sel:[0,1,0]
	v_pk_fma_f32 v[4:5], v[234:235], v[80:81], v[4:5] op_sel_hi:[1,0,1]
	v_pk_fma_f32 v[22:23], v[232:233], v[80:81], v[22:23] op_sel_hi:[1,0,1]
	v_pk_fma_f32 v[24:25], v[234:235], v[102:103], v[24:25] op_sel_hi:[1,0,1]
	v_pk_fma_f32 v[20:21], v[232:233], v[102:103], v[20:21] op_sel_hi:[1,0,1]
	v_pk_fma_f32 v[16:17], v[234:235], v[104:105], v[16:17] op_sel_hi:[1,0,1]
	v_pk_fma_f32 v[18:19], v[232:233], v[104:105], v[18:19] op_sel_hi:[1,0,1]
	v_pk_fma_f32 v[32:33], v[238:239], v[82:83], v[32:33] op_sel_hi:[1,0,1]
	v_pk_fma_f32 v[34:35], v[236:237], v[82:83], v[34:35] op_sel_hi:[1,0,1]
	v_pk_fma_f32 v[6:7], v[238:239], v[82:83], v[6:7] op_sel:[0,1,0]
	v_pk_fma_f32 v[36:37], v[236:237], v[82:83], v[36:37] op_sel:[0,1,0]
	v_pk_fma_f32 v[38:39], v[236:237], v[84:85], v[38:39] op_sel_hi:[1,0,1]
	v_pk_fma_f32 v[8:9], v[238:239], v[84:85], v[8:9] op_sel_hi:[1,0,1]
	v_pk_fma_f32 v[28:29], v[238:239], v[86:87], v[28:29] op_sel_hi:[1,0,1]
	v_pk_fma_f32 v[30:31], v[236:237], v[86:87], v[30:31] op_sel_hi:[1,0,1]
	v_pk_fma_f32 v[2:3], v[238:239], v[86:87], v[2:3] op_sel:[0,1,0]
	v_pk_fma_f32 v[26:27], v[236:237], v[86:87], v[26:27] op_sel:[0,1,0]
	v_pk_fma_f32 v[22:23], v[236:237], v[88:89], v[22:23] op_sel_hi:[1,0,1]
	v_pk_fma_f32 v[4:5], v[238:239], v[88:89], v[4:5] op_sel_hi:[1,0,1]
	v_pk_fma_f32 v[20:21], v[236:237], v[106:107], v[20:21] op_sel_hi:[1,0,1]
	v_pk_fma_f32 v[24:25], v[238:239], v[106:107], v[24:25] op_sel_hi:[1,0,1]
	v_pk_fma_f32 v[18:19], v[236:237], v[108:109], v[18:19] op_sel_hi:[1,0,1]
	v_pk_fma_f32 v[16:17], v[238:239], v[108:109], v[16:17] op_sel_hi:[1,0,1]
	v_pk_fma_f32 v[46:47], v[242:243], v[90:91], v[32:33] op_sel_hi:[1,0,1]
	v_pk_fma_f32 v[48:49], v[240:241], v[90:91], v[34:35] op_sel_hi:[1,0,1]
	v_pk_fma_f32 v[40:41], v[242:243], v[90:91], v[6:7] op_sel:[0,1,0]
	v_pk_fma_f32 v[44:45], v[240:241], v[90:91], v[36:37] op_sel:[0,1,0]
	v_pk_fma_f32 v[36:37], v[242:243], v[92:93], v[8:9] op_sel_hi:[1,0,1]
	v_pk_fma_f32 v[38:39], v[240:241], v[92:93], v[38:39] op_sel_hi:[1,0,1]
	v_pk_fma_f32 v[32:33], v[242:243], v[110:111], v[24:25] op_sel_hi:[1,0,1]
	v_pk_fma_f32 v[34:35], v[240:241], v[110:111], v[20:21] op_sel_hi:[1,0,1]
	v_pk_fma_f32 v[28:29], v[242:243], v[94:95], v[28:29] op_sel_hi:[1,0,1]
	v_pk_fma_f32 v[30:31], v[240:241], v[94:95], v[30:31] op_sel_hi:[1,0,1]
	v_pk_fma_f32 v[24:25], v[242:243], v[94:95], v[2:3] op_sel:[0,1,0]
	v_pk_fma_f32 v[26:27], v[240:241], v[94:95], v[26:27] op_sel:[0,1,0]
	v_pk_fma_f32 v[20:21], v[242:243], v[96:97], v[4:5] op_sel_hi:[1,0,1]
	v_pk_fma_f32 v[22:23], v[240:241], v[96:97], v[22:23] op_sel_hi:[1,0,1]
	v_pk_fma_f32 v[16:17], v[242:243], v[112:113], v[16:17] op_sel_hi:[1,0,1]
	v_pk_fma_f32 v[18:19], v[240:241], v[112:113], v[18:19] op_sel_hi:[1,0,1]
	ds_bpermute_b32 v2, v1, v48
	ds_bpermute_b32 v3, v1, v49
	ds_bpermute_b32 v50, v1, v36
	ds_bpermute_b32 v51, v1, v37
	ds_bpermute_b32 v60, v1, v26
	ds_bpermute_b32 v61, v1, v27
	s_waitcnt lgkmcnt(4)
	v_pk_add_f32 v[2:3], v[48:49], v[2:3]
	ds_bpermute_b32 v48, v1, v40
	ds_bpermute_b32 v49, v1, v41
	s_waitcnt lgkmcnt(4)
	v_pk_add_f32 v[50:51], v[36:37], v[50:51]
	ds_bpermute_b32 v52, v13, v50
	ds_bpermute_b32 v53, v13, v51
	s_waitcnt lgkmcnt(4)
	v_pk_add_f32 v[26:27], v[26:27], v[60:61]
	s_waitcnt lgkmcnt(2)
	v_pk_add_f32 v[40:41], v[40:41], v[48:49]
	ds_bpermute_b32 v48, v1, v38
	ds_bpermute_b32 v49, v1, v39
	ds_bpermute_b32 v64, v1, v22
	ds_bpermute_b32 v65, v1, v23
	ds_bpermute_b32 v4, v1, v46
	ds_bpermute_b32 v5, v1, v47
	s_waitcnt lgkmcnt(4)
; __device__ __forceinline__ void p0_ada(Frame& F, const float* c, const float* ada_w, const float* ada_b, float* mod) {
;     ...
; #pragma unroll
;         for (int b = 0; b < 8; ++b)
; #pragma unroll
;             for (int j = 0; j < 4; ++j) { float v = acc[b][j]; v += __shfl_xor(v, 8); v += __shfl_xor(v, 16); v += __shfl_xor(v, 32); acc[b][j] = v; }
;         if (F.lane < 8) {
; #pragma unroll
;             for (int b = 0; b < 8; ++b) *(f32x4*)(part + (F.wave * 8 + b) * 32 + cq * 4) = acc[b];
;         }
	v_pk_add_f32 v[38:39], v[38:39], v[48:49]
	ds_bpermute_b32 v48, v13, v38
	ds_bpermute_b32 v49, v13, v39
	ds_bpermute_b32 v8, v1, v44
	ds_bpermute_b32 v9, v1, v45
	ds_bpermute_b32 v54, v1, v32
	ds_bpermute_b32 v55, v1, v33
	s_waitcnt lgkmcnt(4)
	v_pk_add_f32 v[36:37], v[38:39], v[48:49]
	v_pk_add_f32 v[48:49], v[50:51], v[52:53]
	ds_bpermute_b32 v52, v1, v34
	ds_bpermute_b32 v53, v1, v35
	ds_bpermute_b32 v58, v1, v30
	ds_bpermute_b32 v59, v1, v31
	ds_bpermute_b32 v62, v13, v26
	ds_bpermute_b32 v63, v13, v27
	ds_bpermute_b32 v6, v13, v2
	ds_bpermute_b32 v7, v13, v3
	v_pk_add_f32 v[22:23], v[22:23], v[64:65]
	v_pk_add_f32 v[42:43], v[46:47], v[4:5]
	s_waitcnt lgkmcnt(10)
	v_pk_add_f32 v[8:9], v[44:45], v[8:9]
	s_waitcnt lgkmcnt(6)
	v_pk_add_f32 v[34:35], v[34:35], v[52:53]
	v_pk_add_f32 v[54:55], v[32:33], v[54:55]
	s_waitcnt lgkmcnt(4)
	v_pk_add_f32 v[30:31], v[30:31], v[58:59]
	ds_bpermute_b32 v58, v1, v28
	ds_bpermute_b32 v59, v1, v29
	s_waitcnt lgkmcnt(4)
	v_pk_add_f32 v[26:27], v[26:27], v[62:63]
	ds_bpermute_b32 v62, v1, v24
	ds_bpermute_b32 v63, v1, v25
	ds_bpermute_b32 v64, v13, v22
	ds_bpermute_b32 v65, v13, v23
	ds_bpermute_b32 v66, v1, v20
	ds_bpermute_b32 v67, v1, v21
	ds_bpermute_b32 v68, v1, v18
	ds_bpermute_b32 v69, v1, v19
	ds_bpermute_b32 v70, v1, v16
	ds_bpermute_b32 v71, v1, v17
	s_waitcnt lgkmcnt(12)
	v_pk_add_f32 v[2:3], v[2:3], v[6:7]
	ds_bpermute_b32 v6, v13, v42
	ds_bpermute_b32 v7, v13, v43
	ds_bpermute_b32 v46, v13, v8
	ds_bpermute_b32 v47, v13, v9
	ds_bpermute_b32 v52, v13, v34
	ds_bpermute_b32 v53, v13, v35
	ds_bpermute_b32 v56, v13, v54
	ds_bpermute_b32 v57, v13, v55
	s_waitcnt lgkmcnt(14)
	v_pk_add_f32 v[28:29], v[28:29], v[58:59]
	v_pk_add_f32 v[24:25], v[24:25], v[62:63]
	v_pk_add_f32 v[22:23], v[22:23], v[64:65]
	s_waitcnt lgkmcnt(12)
	v_pk_add_f32 v[64:65], v[20:21], v[66:67]
	s_waitcnt lgkmcnt(10)
	v_pk_add_f32 v[18:19], v[18:19], v[68:69]
	s_waitcnt lgkmcnt(8)
	v_pk_add_f32 v[70:71], v[16:17], v[70:71]
	s_waitcnt lgkmcnt(6)
	v_pk_add_f32 v[42:43], v[42:43], v[6:7]
	s_waitcnt lgkmcnt(4)
	v_pk_add_f32 v[6:7], v[8:9], v[46:47]
	ds_bpermute_b32 v46, v13, v40
	ds_bpermute_b32 v47, v13, v41
	s_waitcnt lgkmcnt(4)
	v_pk_add_f32 v[32:33], v[34:35], v[52:53]
	s_waitcnt lgkmcnt(2)
	v_pk_add_f32 v[52:53], v[54:55], v[56:57]
	ds_bpermute_b32 v56, v13, v30
	ds_bpermute_b32 v57, v13, v31
	ds_bpermute_b32 v58, v13, v28
	ds_bpermute_b32 v59, v13, v29
	ds_bpermute_b32 v62, v13, v24
	ds_bpermute_b32 v63, v13, v25
	ds_bpermute_b32 v66, v13, v64
	ds_bpermute_b32 v67, v13, v65
	ds_bpermute_b32 v68, v13, v18
	ds_bpermute_b32 v69, v13, v19
	ds_bpermute_b32 v78, v13, v70
	ds_bpermute_b32 v79, v13, v71
	s_waitcnt lgkmcnt(12)
	v_pk_add_f32 v[40:41], v[40:41], v[46:47]
	s_waitcnt lgkmcnt(10)
	v_pk_add_f32 v[30:31], v[30:31], v[56:57]
	s_waitcnt lgkmcnt(8)
	v_pk_add_f32 v[58:59], v[28:29], v[58:59]
	s_waitcnt lgkmcnt(6)
	v_pk_add_f32 v[24:25], v[24:25], v[62:63]
	s_waitcnt lgkmcnt(4)
	v_pk_add_f32 v[64:65], v[64:65], v[66:67]
	s_waitcnt lgkmcnt(2)
	v_pk_add_f32 v[16:17], v[18:19], v[68:69]
	s_waitcnt lgkmcnt(0)
	v_pk_add_f32 v[68:69], v[70:71], v[78:79]
	ds_bpermute_b32 v4, v73, v2
	ds_bpermute_b32 v5, v73, v3
	ds_bpermute_b32 v44, v73, v42
	ds_bpermute_b32 v45, v73, v43
	ds_bpermute_b32 v8, v73, v6
	ds_bpermute_b32 v9, v73, v7
	ds_bpermute_b32 v46, v73, v40
	ds_bpermute_b32 v47, v73, v41
	ds_bpermute_b32 v38, v73, v36
	ds_bpermute_b32 v39, v73, v37
	ds_bpermute_b32 v50, v73, v48
	ds_bpermute_b32 v51, v73, v49
	ds_bpermute_b32 v34, v73, v32
	ds_bpermute_b32 v35, v73, v33
	ds_bpermute_b32 v54, v73, v52
	ds_bpermute_b32 v55, v73, v53
	ds_bpermute_b32 v56, v73, v30
	ds_bpermute_b32 v57, v73, v31
	ds_bpermute_b32 v60, v73, v58
	ds_bpermute_b32 v61, v73, v59
	ds_bpermute_b32 v28, v73, v26
	ds_bpermute_b32 v29, v73, v27
	ds_bpermute_b32 v62, v73, v24
	ds_bpermute_b32 v63, v73, v25
	ds_bpermute_b32 v20, v73, v22
	ds_bpermute_b32 v21, v73, v23
	ds_bpermute_b32 v66, v73, v64
	ds_bpermute_b32 v67, v73, v65
	ds_bpermute_b32 v18, v73, v16
	ds_bpermute_b32 v19, v73, v17
	ds_bpermute_b32 v70, v73, v68
	ds_bpermute_b32 v71, v73, v69
	s_and_saveexec_b64 s[12:13], vcc
	s_cbranch_execz .LBB0_23
	s_waitcnt lgkmcnt(14)
	v_pk_add_f32 v[44:45], v[42:43], v[44:45]
	v_pk_add_f32 v[42:43], v[2:3], v[4:5]
	v_pk_add_f32 v[4:5], v[40:41], v[46:47]
	v_pk_add_f32 v[2:3], v[6:7], v[8:9]
	ds_write_b128 v74, v[2:5] offset:128
	v_pk_add_f32 v[4:5], v[48:49], v[50:51]
	v_pk_add_f32 v[2:3], v[36:37], v[38:39]
	ds_write_b128 v74, v[2:5] offset:256
	v_pk_add_f32 v[4:5], v[52:53], v[54:55]
	v_pk_add_f32 v[2:3], v[32:33], v[34:35]
	ds_write_b128 v74, v[2:5] offset:384
	s_waitcnt lgkmcnt(14)
	v_pk_add_f32 v[4:5], v[58:59], v[60:61]
	v_pk_add_f32 v[2:3], v[30:31], v[56:57]
	ds_write_b128 v74, v[2:5] offset:512
	s_waitcnt lgkmcnt(12)
	v_pk_add_f32 v[4:5], v[24:25], v[62:63]
	v_pk_add_f32 v[2:3], v[26:27], v[28:29]
	ds_write_b128 v74, v[2:5] offset:640
	s_waitcnt lgkmcnt(9)
	v_pk_add_f32 v[4:5], v[64:65], v[66:67]
	v_pk_add_f32 v[2:3], v[22:23], v[20:21]
	ds_write_b128 v74, v[2:5] offset:768
	s_waitcnt lgkmcnt(6)
	v_pk_add_f32 v[4:5], v[68:69], v[70:71]
	v_pk_add_f32 v[2:3], v[16:17], v[18:19]
	ds_write_b128 v74, v[42:45]
	ds_write_b128 v74, v[2:5] offset:896
